# fast path: PV(b)+next QK(a) fused into one 8-slot ring-fed MFMA stream with own mask/loop tail
# speedup vs baseline: 1.0256x; 1.0006x over previous
.Lno_bload2:
	s_add_i32 s98, s10, -1
	s_and_b32 s98, s98, 2
	s_mulk_i32 s98, 0x6000
	v_add_u32_e32 v209, s14, v151
	v_add_u32_e32 v210, s14, v152
	v_add_u32_e32 v213, s14, v153
	v_add_u32_e32 v214, s14, v154
	ds_read_b64_tr_b16 v[224:225], v209
	ds_read_b64_tr_b16 v[226:227], v210 offset:768
	ds_read_b64_tr_b16 v[228:229], v209 offset:128
	ds_read_b64_tr_b16 v[230:231], v210 offset:896
	ds_read_b64_tr_b16 v[232:233], v209 offset:6144
	ds_read_b64_tr_b16 v[234:235], v210 offset:6912
	ds_read_b64_tr_b16 v[236:237], v209 offset:6272
	ds_read_b64_tr_b16 v[238:239], v210 offset:7040
	ds_read_b64_tr_b16 v[240:241], v209 offset:12288
	ds_read_b64_tr_b16 v[242:243], v210 offset:13056
	ds_read_b64_tr_b16 v[244:245], v209 offset:12416
	ds_read_b64_tr_b16 v[246:247], v210 offset:13184
	v_exp_f32_e32 v170, v64
	v_exp_f32_e32 v171, v65
	v_exp_f32_e32 v176, v66
	v_exp_f32_e32 v177, v67
	v_exp_f32_e32 v178, v68
	v_exp_f32_e32 v179, v69
	v_exp_f32_e32 v161, v80
	v_exp_f32_e32 v185, v70
	v_exp_f32_e32 v162, v81
	v_exp_f32_e32 v187, v71
	v_exp_f32_e32 v163, v82
	v_exp_f32_e32 v203, v72
	v_exp_f32_e32 v164, v83
	v_exp_f32_e32 v204, v73
	v_exp_f32_e32 v165, v84
	v_exp_f32_e32 v205, v74
	v_exp_f32_e32 v166, v85
	v_exp_f32_e32 v206, v75
	v_exp_f32_e32 v167, v86
	v_exp_f32_e32 v207, v76
	v_exp_f32_e32 v168, v87
	v_exp_f32_e32 v208, v77
	v_exp_f32_e32 v88, v88
	v_exp_f32_e32 v89, v89
	v_exp_f32_e32 v90, v90
	v_exp_f32_e32 v91, v91
	v_cvt_pk_bf16_f32 v72, v161, v162
	v_cvt_pk_bf16_f32 v73, v165, v166
	v_cvt_pk_bf16_f32 v74, v163, v164
	v_cvt_pk_bf16_f32 v75, v167, v168
	v_exp_f32_e32 v92, v92
	v_exp_f32_e32 v93, v93
	v_exp_f32_e32 v94, v94
	v_exp_f32_e32 v95, v95
	v_exp_f32_e32 v211, v78
	v_mov_b32_e32 v80, v79
	v_cvt_pk_bf16_f32 v76, v88, v89
	v_cvt_pk_bf16_f32 v77, v92, v93
	v_cvt_pk_bf16_f32 v78, v90, v91
	v_cvt_pk_bf16_f32 v79, v94, v95
	v_cvt_pk_bf16_f32 v68, v170, v171
	v_cvt_pk_bf16_f32 v69, v178, v179
	v_cvt_pk_bf16_f32 v70, v176, v177
	v_cvt_pk_bf16_f32 v71, v185, v187
	v_exp_f32_e32 v212, v80
	v_cvt_pk_bf16_f32 v64, v203, v204
	v_cvt_pk_bf16_f32 v65, v207, v208
	v_cvt_pk_bf16_f32 v66, v205, v206
	v_cvt_pk_bf16_f32 v67, v211, v212
	v_add_f32_e32 v158, v158, v159
	s_addk_i32 s12, 0x1000
	s_add_i32 s11, s11, 4
	s_add_i32 s10, s10, 2
	s_addk_i32 s7, 0x80
	v_add_u32_e32 v155, 32, v155
	s_cmp_ge_u32 s13, s9
	v_add_u32_e32 v156, 0xffffff80, v156
	v_add_f32_e32 v84, 0, v161
	v_add_f32_e32 v84, v162, v84
	v_add_f32_e32 v84, v163, v84
	v_add_f32_e32 v84, v164, v84
	v_add_f32_e32 v144, v165, v84
	v_add_f32_e32 v80, v166, v144
	v_add_f32_e32 v80, v167, v80
	v_add_f32_e32 v80, v168, v80
	v_add_f32_e32 v80, v88, v80
	v_add_f32_e32 v88, v89, v80
	v_add_f32_e32 v84, v90, v88
	v_add_f32_e32 v84, v91, v84
	v_add_f32_e32 v84, v92, v84
	v_add_f32_e32 v84, v93, v84
	v_add_f32_e32 v88, v94, v84
	v_add_f32_e32 v80, v95, v88
	v_add_f32_e32 v80, v170, v80
	v_add_f32_e32 v80, v171, v80
	v_add_f32_e32 v80, v176, v80
	v_add_f32_e32 v88, v177, v80
	v_add_f32_e32 v248, v178, v88
	v_add_f32_e32 v249, v179, v248
	v_add_f32_e32 v252, v185, v249
	v_add_f32_e32 v253, v187, v252
	v_add_f32_e32 v84, v203, v253
	v_add_f32_e32 v254, v204, v84
	v_add_f32_e32 v255, v205, v254
	v_add_f32_e32 v248, v206, v255
	v_add_f32_e32 v249, v207, v248
	v_add_f32_e32 v80, v208, v249
	v_add_f32_e32 v252, v211, v80
	v_add_f32_e32 v253, v212, v252
	v_add_f32_e32 v158, v158, v253
	ds_read_b64_tr_b16 v[252:253], v209 offset:18432
	ds_read_b64_tr_b16 v[254:255], v210 offset:19200
	ds_read_b64_tr_b16 v[204:205], v209 offset:18560
	ds_read_b64_tr_b16 v[206:207], v210 offset:19328
	s_barrier
	v_add_u32_e32 v144, s98, v147
	v_add_u32_e32 v146, s98, v148
	v_add_u32_e32 v161, s98, v149
	v_add_u32_e32 v168, s98, v150
	s_waitcnt lgkmcnt(14)
	v_mfma_f32_32x32x16_bf16 v[48:63], v[224:227], v[72:75], v[48:63]
	ds_read_b64_tr_b16 v[224:225], v213
	ds_read_b64_tr_b16 v[226:227], v214 offset:768
	s_waitcnt lgkmcnt(14)
	v_mfma_f32_32x32x16_bf16 v[0:15], v[228:231], v[72:75], v[0:15]
	ds_read_b64_tr_b16 v[228:229], v213 offset:128
	ds_read_b64_tr_b16 v[230:231], v214 offset:896
	s_waitcnt lgkmcnt(14)
	v_mfma_f32_32x32x16_bf16 v[48:63], v[232:235], v[76:79], v[48:63]
	ds_read_b64_tr_b16 v[232:233], v213 offset:6144
	ds_read_b64_tr_b16 v[234:235], v214 offset:6912
	s_waitcnt lgkmcnt(14)
	v_mfma_f32_32x32x16_bf16 v[0:15], v[236:239], v[76:79], v[0:15]
	ds_read_b64_tr_b16 v[236:237], v213 offset:6272
	ds_read_b64_tr_b16 v[238:239], v214 offset:7040
	s_waitcnt lgkmcnt(14)
	v_mfma_f32_32x32x16_bf16 v[48:63], v[240:243], v[68:71], v[48:63]
	ds_read_b64_tr_b16 v[240:241], v213 offset:12288
	ds_read_b64_tr_b16 v[242:243], v214 offset:13056
	s_waitcnt lgkmcnt(14)
	v_mfma_f32_32x32x16_bf16 v[0:15], v[244:247], v[68:71], v[0:15]
	ds_read_b64_tr_b16 v[244:245], v213 offset:12416
	ds_read_b64_tr_b16 v[246:247], v214 offset:13184
	s_waitcnt lgkmcnt(14)
	v_mfma_f32_32x32x16_bf16 v[48:63], v[252:255], v[64:67], v[48:63]
	ds_read_b64_tr_b16 v[252:253], v213 offset:18432
	ds_read_b64_tr_b16 v[254:255], v214 offset:19200
	s_waitcnt lgkmcnt(14)
	v_mfma_f32_32x32x16_bf16 v[0:15], v[204:207], v[64:67], v[0:15]
	ds_read_b64_tr_b16 v[204:205], v213 offset:18560
	ds_read_b64_tr_b16 v[206:207], v214 offset:19328
	s_waitcnt lgkmcnt(14)
	v_mfma_f32_32x32x16_bf16 v[32:47], v[224:227], v[72:75], v[32:47]
	ds_read_b128 v[224:227], v144
	s_waitcnt lgkmcnt(13)
	v_mfma_f32_32x32x16_bf16 v[16:31], v[228:231], v[72:75], v[16:31]
	ds_read_b128 v[228:231], v144 offset:12288
	s_waitcnt lgkmcnt(12)
	v_mfma_f32_32x32x16_bf16 v[32:47], v[232:235], v[76:79], v[32:47]
	ds_read_b128 v[232:235], v146
	s_waitcnt lgkmcnt(11)
	v_mfma_f32_32x32x16_bf16 v[16:31], v[236:239], v[76:79], v[16:31]
	ds_read_b128 v[236:239], v146 offset:12288
	s_waitcnt lgkmcnt(10)
	v_mfma_f32_32x32x16_bf16 v[32:47], v[240:243], v[68:71], v[32:47]
	ds_read_b128 v[240:243], v161
	s_waitcnt lgkmcnt(9)
	v_mfma_f32_32x32x16_bf16 v[16:31], v[244:247], v[68:71], v[16:31]
	ds_read_b128 v[244:247], v161 offset:12288
	s_waitcnt lgkmcnt(8)
	v_mfma_f32_32x32x16_bf16 v[32:47], v[252:255], v[64:67], v[32:47]
	ds_read_b128 v[252:255], v168
	s_waitcnt lgkmcnt(7)
	v_mfma_f32_32x32x16_bf16 v[16:31], v[204:207], v[64:67], v[16:31]
	ds_read_b128 v[204:207], v168 offset:12288
	s_cbranch_scc1 .LBB0_1250
	s_add_i32 s13, s10, -1
	s_mov_b32 s14, s98
	s_waitcnt lgkmcnt(7)
	v_mfma_f32_32x32x16_bf16 v[80:95], v[224:227], v[112:115], 0
	ds_read_b128 v[224:227], v144 offset:128
	s_waitcnt lgkmcnt(7)
	v_mfma_f32_32x32x16_bf16 v[64:79], v[228:231], v[112:115], 0
	ds_read_b128 v[228:231], v144 offset:12416
	s_waitcnt lgkmcnt(7)
	v_mfma_f32_32x32x16_bf16 v[80:95], v[232:235], v[116:119], v[80:95]
	ds_read_b128 v[232:235], v146 offset:128
	s_waitcnt lgkmcnt(7)
	v_mfma_f32_32x32x16_bf16 v[64:79], v[236:239], v[116:119], v[64:79]
	ds_read_b128 v[236:239], v146 offset:12416
	s_waitcnt lgkmcnt(7)
	v_mfma_f32_32x32x16_bf16 v[80:95], v[240:243], v[120:123], v[80:95]
	ds_read_b128 v[240:243], v161 offset:128
	s_waitcnt lgkmcnt(7)
	v_mfma_f32_32x32x16_bf16 v[64:79], v[244:247], v[120:123], v[64:79]
	ds_read_b128 v[244:247], v161 offset:12416
	s_waitcnt lgkmcnt(7)
	v_mfma_f32_32x32x16_bf16 v[80:95], v[252:255], v[124:127], v[80:95]
	ds_read_b128 v[252:255], v168 offset:128
	s_waitcnt lgkmcnt(7)
	v_mfma_f32_32x32x16_bf16 v[64:79], v[204:207], v[124:127], v[64:79]
	ds_read_b128 v[204:207], v168 offset:12416
	s_waitcnt lgkmcnt(7)
	v_mfma_f32_32x32x16_bf16 v[80:95], v[224:227], v[96:99], v[80:95]
	ds_read_b128 v[224:227], v144 offset:256
	s_waitcnt lgkmcnt(7)
	v_mfma_f32_32x32x16_bf16 v[64:79], v[228:231], v[96:99], v[64:79]
	ds_read_b128 v[228:231], v144 offset:12544
	s_waitcnt lgkmcnt(7)
	v_mfma_f32_32x32x16_bf16 v[80:95], v[232:235], v[100:103], v[80:95]
	ds_read_b128 v[232:235], v146 offset:256
	s_waitcnt lgkmcnt(7)
	v_mfma_f32_32x32x16_bf16 v[64:79], v[236:239], v[100:103], v[64:79]
	ds_read_b128 v[236:239], v146 offset:12544
	s_waitcnt lgkmcnt(7)
	v_mfma_f32_32x32x16_bf16 v[80:95], v[240:243], v[104:107], v[80:95]
	ds_read_b128 v[240:243], v161 offset:256
	s_waitcnt lgkmcnt(7)
	v_mfma_f32_32x32x16_bf16 v[64:79], v[244:247], v[104:107], v[64:79]
	ds_read_b128 v[244:247], v161 offset:12544
	s_waitcnt lgkmcnt(7)
	v_mfma_f32_32x32x16_bf16 v[80:95], v[252:255], v[108:111], v[80:95]
	ds_read_b128 v[252:255], v168 offset:256
	s_waitcnt lgkmcnt(7)
	v_mfma_f32_32x32x16_bf16 v[64:79], v[204:207], v[108:111], v[64:79]
	ds_read_b128 v[204:207], v168 offset:12544
	s_waitcnt lgkmcnt(7)
	v_mfma_f32_32x32x16_bf16 v[80:95], v[224:227], v[128:131], v[80:95]
	s_waitcnt lgkmcnt(6)
	v_mfma_f32_32x32x16_bf16 v[64:79], v[228:231], v[128:131], v[64:79]
	s_waitcnt lgkmcnt(5)
	v_mfma_f32_32x32x16_bf16 v[80:95], v[232:235], v[132:135], v[80:95]
	s_waitcnt lgkmcnt(4)
	v_mfma_f32_32x32x16_bf16 v[64:79], v[236:239], v[132:135], v[64:79]
	s_waitcnt lgkmcnt(3)
	v_mfma_f32_32x32x16_bf16 v[80:95], v[240:243], v[136:139], v[80:95]
	s_waitcnt lgkmcnt(2)
	v_mfma_f32_32x32x16_bf16 v[64:79], v[244:247], v[136:139], v[64:79]
	s_waitcnt lgkmcnt(1)
	v_mfma_f32_32x32x16_bf16 v[80:95], v[252:255], v[140:143], v[80:95]
	s_waitcnt lgkmcnt(0)
	v_mfma_f32_32x32x16_bf16 v[64:79], v[204:207], v[140:143], v[64:79]
	s_waitcnt vmcnt(0)
	s_barrier
	s_sub_i32 s15, s7, 64
	s_cmp_le_u32 s15, s44
	s_cbranch_scc1 .Lf_a
	v_add_u32_e32 v144, 123, v156
	v_cmp_le_i32_e64 s[16:17], 0, v144
	v_cmp_le_i32_e64 s[18:19], 32, v144
	v_cmp_le_i32_e64 vcc, 1, v144
	s_nop 4
	v_cndmask_b32_e64 v80, v199, v80, s[16:17]
	v_cmp_le_i32_e64 s[16:17], 33, v144
	v_cndmask_b32_e64 v64, v199, v64, s[18:19]
	v_cmp_le_i32_e64 s[18:19], 2, v144
	v_cndmask_b32_e64 v81, v199, v81, vcc
	v_cmp_le_i32_e64 vcc, 34, v144
	v_cndmask_b32_e64 v65, v199, v65, s[16:17]
	v_cmp_le_i32_e64 s[16:17], 3, v144
	v_cndmask_b32_e64 v82, v199, v82, s[18:19]
	v_cmp_le_i32_e64 s[18:19], 35, v144
	v_cndmask_b32_e64 v66, v199, v66, vcc
	v_cmp_le_i32_e64 vcc, 8, v144
	v_cndmask_b32_e64 v83, v199, v83, s[16:17]
	v_cmp_le_i32_e64 s[16:17], 40, v144
	v_cndmask_b32_e64 v67, v199, v67, s[18:19]
	v_cmp_le_i32_e64 s[18:19], 9, v144
	v_cndmask_b32_e64 v84, v199, v84, vcc
	v_cmp_le_i32_e64 vcc, 41, v144
	v_cndmask_b32_e64 v68, v199, v68, s[16:17]
	v_cmp_le_i32_e64 s[16:17], 10, v144
	v_cndmask_b32_e64 v85, v199, v85, s[18:19]
	v_cmp_le_i32_e64 s[18:19], 42, v144
	v_cndmask_b32_e64 v69, v199, v69, vcc
	v_cmp_le_i32_e64 vcc, 11, v144
	v_cndmask_b32_e64 v86, v199, v86, s[16:17]
	v_cmp_le_i32_e64 s[16:17], 43, v144
	v_cndmask_b32_e64 v70, v199, v70, s[18:19]
	v_cmp_le_i32_e64 s[18:19], 16, v144
	v_cndmask_b32_e64 v87, v199, v87, vcc
	v_cmp_le_i32_e64 vcc, 48, v144
	v_cndmask_b32_e64 v71, v199, v71, s[16:17]
	v_cmp_le_i32_e64 s[16:17], 17, v144
	v_cndmask_b32_e64 v88, v199, v88, s[18:19]
	v_cmp_le_i32_e64 s[18:19], 49, v144
	v_cndmask_b32_e64 v72, v199, v72, vcc
	v_cmp_le_i32_e64 vcc, 18, v144
	v_cndmask_b32_e64 v89, v199, v89, s[16:17]
	v_cmp_le_i32_e64 s[16:17], 50, v144
	v_cndmask_b32_e64 v73, v199, v73, s[18:19]
	v_cmp_le_i32_e64 s[18:19], 19, v144
	v_cndmask_b32_e64 v90, v199, v90, vcc
	v_cmp_le_i32_e64 vcc, 51, v144
	v_cndmask_b32_e64 v74, v199, v74, s[16:17]
	v_cmp_le_i32_e64 s[16:17], 24, v144
	v_cndmask_b32_e64 v91, v199, v91, s[18:19]
	v_cmp_le_i32_e64 s[18:19], 56, v144
	v_cndmask_b32_e64 v75, v199, v75, vcc
	v_cmp_le_i32_e64 vcc, 25, v144
	v_cndmask_b32_e64 v92, v199, v92, s[16:17]
	v_cmp_le_i32_e64 s[16:17], 57, v144
	v_cndmask_b32_e64 v76, v199, v76, s[18:19]
	v_cmp_le_i32_e64 s[18:19], 26, v144
	v_cndmask_b32_e64 v93, v199, v93, vcc
	v_cmp_le_i32_e64 vcc, 58, v144
	v_cndmask_b32_e64 v77, v199, v77, s[16:17]
	v_cmp_le_i32_e64 s[16:17], 27, v144
	v_cndmask_b32_e64 v94, v199, v94, s[18:19]
	v_cmp_le_i32_e64 s[18:19], 59, v144
	v_cndmask_b32_e64 v78, v199, v78, vcc
	v_cndmask_b32_e64 v95, v199, v95, s[16:17]
	v_cndmask_b32_e64 v79, v199, v79, s[18:19]
	s_branch .Lf_a
.LBB0_1250:
	s_waitcnt vmcnt(0) lgkmcnt(0)
	s_cmp_eq_u32 s101, 0
	s_cbranch_scc1 .Lnostag_out
	s_cmp_ge_u32 s88, 0x1000
	s_cbranch_scc1 .Lnostag_out
	s_barrier
